# P9 (down proj) epilogue software-pipelined: g2 hoisted, x1 loads 4 sub-chunks ahead, counted vmcnt (on top of v39)
# speedup vs baseline: 1.0020x; 1.0020x over previous
.LBB0_1861:
	s_lshr_b32 s0, s49, 5
	s_mul_i32 s26, s0, 0x1800
	s_ashr_i32 s27, s26, 31
	s_lshl_b32 s24, s48, 2
	v_lshl_add_u32 v146, s49, 8, v150
	s_ashr_i32 s25, s24, 31
	s_lshl_b64 s[26:27], s[26:27], 2
	v_lshl_or_b32 v170, s48, 8, v152
	v_ashrrev_i32_e32 v147, 31, v146
	s_add_u32 s0, s96, s26
	v_lshlrev_b64 v[172:173], 11, v[146:147]
	v_ashrrev_i32_e32 v171, 31, v170
	s_addc_u32 s27, s97, s27
	v_lshlrev_b64 v[144:145], 1, v[170:171]
	s_add_u32 s26, s0, 0x5000
	s_addc_u32 s27, s27, 0
	v_lshl_add_u64 v[148:149], v[170:171], 2, s[26:27]
	global_load_dwordx4 v[202:205], v[148:149], off
	global_load_dwordx4 v[206:209], v[148:149], off offset:16
	global_load_dwordx4 v[210:213], v[148:149], off offset:512
	global_load_dwordx4 v[214:217], v[148:149], off offset:528
	v_lshl_add_u64 v[182:183], s[12:13], 0, v[172:173]
	v_lshl_add_u64 v[182:183], v[182:183], 0, v[144:145]
	v_lshl_add_u64 v[184:185], s[14:15], 0, v[172:173]
	v_lshl_add_u64 v[184:185], v[184:185], 0, v[144:145]
	global_load_dwordx4 v[158:161], v[182:183], off
	global_load_dwordx4 v[162:165], v[182:183], off offset:256
	v_add_co_u32_e32 v182, vcc, 0x8000, v182
	s_nop 1
	v_addc_co_u32_e32 v183, vcc, 0, v183, vcc
	global_load_dwordx4 v[166:169], v[182:183], off
	global_load_dwordx4 v[170:173], v[182:183], off offset:256
	v_lshlrev_b64 v[186:187], 6, v[146:147]
	v_lshl_add_u64 v[186:187], s[16:17], 0, v[186:187]
	v_lshl_add_u64 v[186:187], s[24:25], 2, v[186:187]
	s_lshl_b32 s0, s38, 2
	v_lshl_add_u64 v[186:187], v[186:187], 0, s[0:1]
	v_add_co_u32_e32 v188, vcc, 0x2000, v186
	s_nop 1
	v_addc_co_u32_e32 v189, vcc, 0, v187, vcc
	v_and_b32_e32 v193, 64, v156
	v_add_u32_e32 v193, 64, v193
	v_xor_b32_e32 v192, 16, v156
	v_cmp_lt_i32_e32 vcc, v192, v193
	s_nop 1
	v_cndmask_b32_e32 v192, v156, v192, vcc
	v_lshlrev_b32_e32 v190, 2, v192
	v_xor_b32_e32 v192, 32, v156
	v_cmp_lt_i32_e32 vcc, v192, v193
	s_nop 1
	v_cndmask_b32_e32 v192, v156, v192, vcc
	v_lshlrev_b32_e32 v191, 2, v192
	s_waitcnt vmcnt(3)
	v_lshlrev_b32_e32 v174, 16, v158
	v_and_b32_e32 v175, 0xffff0000, v158
	v_lshlrev_b32_e32 v176, 16, v159
	v_and_b32_e32 v177, 0xffff0000, v159
	v_lshlrev_b32_e32 v178, 16, v160
	v_and_b32_e32 v179, 0xffff0000, v160
	v_lshlrev_b32_e32 v180, 16, v161
	v_and_b32_e32 v181, 0xffff0000, v161
	v_add_co_u32_e32 v182, vcc, 0x8000, v182
	s_nop 1
	v_addc_co_u32_e32 v183, vcc, 0, v183, vcc
	global_load_dwordx4 v[158:161], v[182:183], off
	v_pk_fma_f32 v[174:175], v[124:125], v[202:203], v[174:175]
	v_pk_fma_f32 v[176:177], v[126:127], v[204:205], v[176:177]
	v_pk_fma_f32 v[178:179], v[120:121], v[206:207], v[178:179]
	v_pk_fma_f32 v[180:181], v[122:123], v[208:209], v[180:181]
	v_cvt_pk_bf16_f32 v120, v174, v175
	v_cvt_pk_bf16_f32 v121, v176, v177
	v_cvt_pk_bf16_f32 v122, v178, v179
	v_cvt_pk_bf16_f32 v123, v180, v181
	global_store_dwordx4 v[184:185], v[120:123], off
	v_mul_f32_e32 v124, v175, v175
	v_fmac_f32_e32 v124, v174, v174
	v_mul_f32_e32 v125, v177, v177
	v_fmac_f32_e32 v125, v176, v176
	v_mul_f32_e32 v126, v179, v179
	v_fmac_f32_e32 v126, v178, v178
	v_mul_f32_e32 v127, v181, v181
	v_fmac_f32_e32 v127, v180, v180
	v_add_f32_e32 v124, v124, v125
	v_add_f32_e32 v124, v126, v124
	v_add_f32_e32 v124, v127, v124
	v_mov_b32_e32 v192, v124
	s_waitcnt vmcnt(4)
	v_lshlrev_b32_e32 v174, 16, v162
	v_and_b32_e32 v175, 0xffff0000, v162
	v_lshlrev_b32_e32 v176, 16, v163
	v_and_b32_e32 v177, 0xffff0000, v163
	v_lshlrev_b32_e32 v178, 16, v164
	v_and_b32_e32 v179, 0xffff0000, v164
	v_lshlrev_b32_e32 v180, 16, v165
	v_and_b32_e32 v181, 0xffff0000, v165
	global_load_dwordx4 v[162:165], v[182:183], off offset:256
	v_pk_fma_f32 v[174:175], v[116:117], v[210:211], v[174:175]
	v_pk_fma_f32 v[176:177], v[118:119], v[212:213], v[176:177]
	v_pk_fma_f32 v[178:179], v[112:113], v[214:215], v[178:179]
	v_pk_fma_f32 v[180:181], v[114:115], v[216:217], v[180:181]
	v_cvt_pk_bf16_f32 v112, v174, v175
	v_cvt_pk_bf16_f32 v113, v176, v177
	v_cvt_pk_bf16_f32 v114, v178, v179
	v_cvt_pk_bf16_f32 v115, v180, v181
	global_store_dwordx4 v[184:185], v[112:115], off offset:256
	v_mul_f32_e32 v116, v175, v175
	v_fmac_f32_e32 v116, v174, v174
	v_mul_f32_e32 v117, v177, v177
	v_fmac_f32_e32 v117, v176, v176
	v_mul_f32_e32 v118, v179, v179
	v_fmac_f32_e32 v118, v178, v178
	v_mul_f32_e32 v119, v181, v181
	v_fmac_f32_e32 v119, v180, v180
	v_add_f32_e32 v116, v116, v117
	v_add_f32_e32 v116, v118, v116
	v_add_f32_e32 v116, v119, v116
	v_add_f32_e32 v192, v192, v116
	ds_bpermute_b32 v193, v190, v192
	s_waitcnt lgkmcnt(0)
	v_add_f32_e32 v192, v192, v193
	ds_bpermute_b32 v193, v191, v192
	s_waitcnt lgkmcnt(0)
	v_add_f32_e32 v192, v192, v193
	s_and_saveexec_b64 s[26:27], s[4:5]
	global_store_dword v[186:187], v192, off
	s_or_b64 exec, exec, s[26:27]
	v_add_co_u32_e32 v184, vcc, 0x8000, v184
	s_nop 1
	v_addc_co_u32_e32 v185, vcc, 0, v185, vcc
	s_waitcnt vmcnt(6)
	v_lshlrev_b32_e32 v174, 16, v166
	v_and_b32_e32 v175, 0xffff0000, v166
	v_lshlrev_b32_e32 v176, 16, v167
	v_and_b32_e32 v177, 0xffff0000, v167
	v_lshlrev_b32_e32 v178, 16, v168
	v_and_b32_e32 v179, 0xffff0000, v168
	v_lshlrev_b32_e32 v180, 16, v169
	v_and_b32_e32 v181, 0xffff0000, v169
	v_add_co_u32_e32 v182, vcc, 0x8000, v182
	s_nop 1
	v_addc_co_u32_e32 v183, vcc, 0, v183, vcc
	global_load_dwordx4 v[166:169], v[182:183], off
	v_pk_fma_f32 v[174:175], v[108:109], v[202:203], v[174:175]
	v_pk_fma_f32 v[176:177], v[110:111], v[204:205], v[176:177]
	v_pk_fma_f32 v[178:179], v[104:105], v[206:207], v[178:179]
	v_pk_fma_f32 v[180:181], v[106:107], v[208:209], v[180:181]
	v_cvt_pk_bf16_f32 v104, v174, v175
	v_cvt_pk_bf16_f32 v105, v176, v177
	v_cvt_pk_bf16_f32 v106, v178, v179
	v_cvt_pk_bf16_f32 v107, v180, v181
	global_store_dwordx4 v[184:185], v[104:107], off
	v_mul_f32_e32 v108, v175, v175
	v_fmac_f32_e32 v108, v174, v174
	v_mul_f32_e32 v109, v177, v177
	v_fmac_f32_e32 v109, v176, v176
	v_mul_f32_e32 v110, v179, v179
	v_fmac_f32_e32 v110, v178, v178
	v_mul_f32_e32 v111, v181, v181
	v_fmac_f32_e32 v111, v180, v180
	v_add_f32_e32 v108, v108, v109
	v_add_f32_e32 v108, v110, v108
	v_add_f32_e32 v108, v111, v108
	v_mov_b32_e32 v192, v108
	s_waitcnt vmcnt(7)
	v_lshlrev_b32_e32 v174, 16, v170
	v_and_b32_e32 v175, 0xffff0000, v170
	v_lshlrev_b32_e32 v176, 16, v171
	v_and_b32_e32 v177, 0xffff0000, v171
	v_lshlrev_b32_e32 v178, 16, v172
	v_and_b32_e32 v179, 0xffff0000, v172
	v_lshlrev_b32_e32 v180, 16, v173
	v_and_b32_e32 v181, 0xffff0000, v173
	global_load_dwordx4 v[170:173], v[182:183], off offset:256
	v_pk_fma_f32 v[174:175], v[100:101], v[210:211], v[174:175]
	v_pk_fma_f32 v[176:177], v[102:103], v[212:213], v[176:177]
	v_pk_fma_f32 v[178:179], v[96:97], v[214:215], v[178:179]
	v_pk_fma_f32 v[180:181], v[98:99], v[216:217], v[180:181]
	v_cvt_pk_bf16_f32 v96, v174, v175
	v_cvt_pk_bf16_f32 v97, v176, v177
	v_cvt_pk_bf16_f32 v98, v178, v179
	v_cvt_pk_bf16_f32 v99, v180, v181
	global_store_dwordx4 v[184:185], v[96:99], off offset:256
	v_mul_f32_e32 v100, v175, v175
	v_fmac_f32_e32 v100, v174, v174
	v_mul_f32_e32 v101, v177, v177
	v_fmac_f32_e32 v101, v176, v176
	v_mul_f32_e32 v102, v179, v179
	v_fmac_f32_e32 v102, v178, v178
	v_mul_f32_e32 v103, v181, v181
	v_fmac_f32_e32 v103, v180, v180
	v_add_f32_e32 v100, v100, v101
	v_add_f32_e32 v100, v102, v100
	v_add_f32_e32 v100, v103, v100
	v_add_f32_e32 v192, v192, v100
	ds_bpermute_b32 v193, v190, v192
	s_waitcnt lgkmcnt(0)
	v_add_f32_e32 v192, v192, v193
	ds_bpermute_b32 v193, v191, v192
	s_waitcnt lgkmcnt(0)
	v_add_f32_e32 v192, v192, v193
	s_and_saveexec_b64 s[26:27], s[4:5]
	global_store_dword v[186:187], v192, off offset:1024
	s_or_b64 exec, exec, s[26:27]
	v_add_co_u32_e32 v184, vcc, 0x8000, v184
	s_nop 1
	v_addc_co_u32_e32 v185, vcc, 0, v185, vcc
	s_waitcnt vmcnt(9)
	v_lshlrev_b32_e32 v174, 16, v158
	v_and_b32_e32 v175, 0xffff0000, v158
	v_lshlrev_b32_e32 v176, 16, v159
	v_and_b32_e32 v177, 0xffff0000, v159
	v_lshlrev_b32_e32 v178, 16, v160
	v_and_b32_e32 v179, 0xffff0000, v160
	v_lshlrev_b32_e32 v180, 16, v161
	v_and_b32_e32 v181, 0xffff0000, v161
	v_add_co_u32_e32 v182, vcc, 0x28000, v182
	s_nop 1
	v_addc_co_u32_e32 v183, vcc, 0, v183, vcc
	global_load_dwordx4 v[158:161], v[182:183], off
	v_pk_fma_f32 v[174:175], v[92:93], v[202:203], v[174:175]
	v_pk_fma_f32 v[176:177], v[94:95], v[204:205], v[176:177]
	v_pk_fma_f32 v[178:179], v[88:89], v[206:207], v[178:179]
	v_pk_fma_f32 v[180:181], v[90:91], v[208:209], v[180:181]
	v_cvt_pk_bf16_f32 v88, v174, v175
	v_cvt_pk_bf16_f32 v89, v176, v177
	v_cvt_pk_bf16_f32 v90, v178, v179
	v_cvt_pk_bf16_f32 v91, v180, v181
	global_store_dwordx4 v[184:185], v[88:91], off
	v_mul_f32_e32 v92, v175, v175
	v_fmac_f32_e32 v92, v174, v174
	v_mul_f32_e32 v93, v177, v177
	v_fmac_f32_e32 v93, v176, v176
	v_mul_f32_e32 v94, v179, v179
	v_fmac_f32_e32 v94, v178, v178
	v_mul_f32_e32 v95, v181, v181
	v_fmac_f32_e32 v95, v180, v180
	v_add_f32_e32 v92, v92, v93
	v_add_f32_e32 v92, v94, v92
	v_add_f32_e32 v92, v95, v92
	v_mov_b32_e32 v192, v92
	s_waitcnt vmcnt(9)
	v_lshlrev_b32_e32 v174, 16, v162
	v_and_b32_e32 v175, 0xffff0000, v162
	v_lshlrev_b32_e32 v176, 16, v163
	v_and_b32_e32 v177, 0xffff0000, v163
	v_lshlrev_b32_e32 v178, 16, v164
	v_and_b32_e32 v179, 0xffff0000, v164
	v_lshlrev_b32_e32 v180, 16, v165
	v_and_b32_e32 v181, 0xffff0000, v165
	global_load_dwordx4 v[162:165], v[182:183], off offset:256
	v_pk_fma_f32 v[174:175], v[84:85], v[210:211], v[174:175]
	v_pk_fma_f32 v[176:177], v[86:87], v[212:213], v[176:177]
	v_pk_fma_f32 v[178:179], v[80:81], v[214:215], v[178:179]
	v_pk_fma_f32 v[180:181], v[82:83], v[216:217], v[180:181]
	v_cvt_pk_bf16_f32 v80, v174, v175
	v_cvt_pk_bf16_f32 v81, v176, v177
	v_cvt_pk_bf16_f32 v82, v178, v179
	v_cvt_pk_bf16_f32 v83, v180, v181
	global_store_dwordx4 v[184:185], v[80:83], off offset:256
	v_mul_f32_e32 v84, v175, v175
	v_fmac_f32_e32 v84, v174, v174
	v_mul_f32_e32 v85, v177, v177
	v_fmac_f32_e32 v85, v176, v176
	v_mul_f32_e32 v86, v179, v179
	v_fmac_f32_e32 v86, v178, v178
	v_mul_f32_e32 v87, v181, v181
	v_fmac_f32_e32 v87, v180, v180
	v_add_f32_e32 v84, v84, v85
	v_add_f32_e32 v84, v86, v84
	v_add_f32_e32 v84, v87, v84
	v_add_f32_e32 v192, v192, v84
	ds_bpermute_b32 v193, v190, v192
	s_waitcnt lgkmcnt(0)
	v_add_f32_e32 v192, v192, v193
	ds_bpermute_b32 v193, v191, v192
	s_waitcnt lgkmcnt(0)
	v_add_f32_e32 v192, v192, v193
	s_and_saveexec_b64 s[26:27], s[4:5]
	global_store_dword v[186:187], v192, off offset:2048
	s_or_b64 exec, exec, s[26:27]
	v_add_co_u32_e32 v184, vcc, 0x8000, v184
	s_nop 1
	v_addc_co_u32_e32 v185, vcc, 0, v185, vcc
	s_waitcnt vmcnt(9)
	v_lshlrev_b32_e32 v174, 16, v166
	v_and_b32_e32 v175, 0xffff0000, v166
	v_lshlrev_b32_e32 v176, 16, v167
	v_and_b32_e32 v177, 0xffff0000, v167
	v_lshlrev_b32_e32 v178, 16, v168
	v_and_b32_e32 v179, 0xffff0000, v168
	v_lshlrev_b32_e32 v180, 16, v169
	v_and_b32_e32 v181, 0xffff0000, v169
	v_add_co_u32_e32 v182, vcc, 0x8000, v182
	s_nop 1
	v_addc_co_u32_e32 v183, vcc, 0, v183, vcc
	global_load_dwordx4 v[166:169], v[182:183], off
	v_pk_fma_f32 v[174:175], v[76:77], v[202:203], v[174:175]
	v_pk_fma_f32 v[176:177], v[78:79], v[204:205], v[176:177]
	v_pk_fma_f32 v[178:179], v[72:73], v[206:207], v[178:179]
	v_pk_fma_f32 v[180:181], v[74:75], v[208:209], v[180:181]
	v_cvt_pk_bf16_f32 v72, v174, v175
	v_cvt_pk_bf16_f32 v73, v176, v177
	v_cvt_pk_bf16_f32 v74, v178, v179
	v_cvt_pk_bf16_f32 v75, v180, v181
	global_store_dwordx4 v[184:185], v[72:75], off
	v_mul_f32_e32 v76, v175, v175
	v_fmac_f32_e32 v76, v174, v174
	v_mul_f32_e32 v77, v177, v177
	v_fmac_f32_e32 v77, v176, v176
	v_mul_f32_e32 v78, v179, v179
	v_fmac_f32_e32 v78, v178, v178
	v_mul_f32_e32 v79, v181, v181
	v_fmac_f32_e32 v79, v180, v180
	v_add_f32_e32 v76, v76, v77
	v_add_f32_e32 v76, v78, v76
	v_add_f32_e32 v76, v79, v76
	v_mov_b32_e32 v192, v76
	s_waitcnt vmcnt(9)
	v_lshlrev_b32_e32 v174, 16, v170
	v_and_b32_e32 v175, 0xffff0000, v170
	v_lshlrev_b32_e32 v176, 16, v171
	v_and_b32_e32 v177, 0xffff0000, v171
	v_lshlrev_b32_e32 v178, 16, v172
	v_and_b32_e32 v179, 0xffff0000, v172
	v_lshlrev_b32_e32 v180, 16, v173
	v_and_b32_e32 v181, 0xffff0000, v173
	global_load_dwordx4 v[170:173], v[182:183], off offset:256
	v_pk_fma_f32 v[174:175], v[68:69], v[210:211], v[174:175]
	v_pk_fma_f32 v[176:177], v[70:71], v[212:213], v[176:177]
	v_pk_fma_f32 v[178:179], v[64:65], v[214:215], v[178:179]
	v_pk_fma_f32 v[180:181], v[66:67], v[216:217], v[180:181]
	v_cvt_pk_bf16_f32 v64, v174, v175
	v_cvt_pk_bf16_f32 v65, v176, v177
	v_cvt_pk_bf16_f32 v66, v178, v179
	v_cvt_pk_bf16_f32 v67, v180, v181
	global_store_dwordx4 v[184:185], v[64:67], off offset:256
	v_mul_f32_e32 v68, v175, v175
	v_fmac_f32_e32 v68, v174, v174
	v_mul_f32_e32 v69, v177, v177
	v_fmac_f32_e32 v69, v176, v176
	v_mul_f32_e32 v70, v179, v179
	v_fmac_f32_e32 v70, v178, v178
	v_mul_f32_e32 v71, v181, v181
	v_fmac_f32_e32 v71, v180, v180
	v_add_f32_e32 v68, v68, v69
	v_add_f32_e32 v68, v70, v68
	v_add_f32_e32 v68, v71, v68
	v_add_f32_e32 v192, v192, v68
	ds_bpermute_b32 v193, v190, v192
	s_waitcnt lgkmcnt(0)
	v_add_f32_e32 v192, v192, v193
	ds_bpermute_b32 v193, v191, v192
	s_waitcnt lgkmcnt(0)
	v_add_f32_e32 v192, v192, v193
	s_and_saveexec_b64 s[26:27], s[4:5]
	global_store_dword v[186:187], v192, off offset:3072
	s_or_b64 exec, exec, s[26:27]
	v_add_co_u32_e32 v184, vcc, 0x28000, v184
	s_nop 1
	v_addc_co_u32_e32 v185, vcc, 0, v185, vcc
	s_waitcnt vmcnt(9)
	v_lshlrev_b32_e32 v174, 16, v158
	v_and_b32_e32 v175, 0xffff0000, v158
	v_lshlrev_b32_e32 v176, 16, v159
	v_and_b32_e32 v177, 0xffff0000, v159
	v_lshlrev_b32_e32 v178, 16, v160
	v_and_b32_e32 v179, 0xffff0000, v160
	v_lshlrev_b32_e32 v180, 16, v161
	v_and_b32_e32 v181, 0xffff0000, v161
	v_add_co_u32_e32 v182, vcc, 0x8000, v182
	s_nop 1
	v_addc_co_u32_e32 v183, vcc, 0, v183, vcc
	global_load_dwordx4 v[158:161], v[182:183], off
	v_pk_fma_f32 v[174:175], v[60:61], v[202:203], v[174:175]
	v_pk_fma_f32 v[176:177], v[62:63], v[204:205], v[176:177]
	v_pk_fma_f32 v[178:179], v[56:57], v[206:207], v[178:179]
	v_pk_fma_f32 v[180:181], v[58:59], v[208:209], v[180:181]
	v_cvt_pk_bf16_f32 v56, v174, v175
	v_cvt_pk_bf16_f32 v57, v176, v177
	v_cvt_pk_bf16_f32 v58, v178, v179
	v_cvt_pk_bf16_f32 v59, v180, v181
	global_store_dwordx4 v[184:185], v[56:59], off
	v_mul_f32_e32 v60, v175, v175
	v_fmac_f32_e32 v60, v174, v174
	v_mul_f32_e32 v61, v177, v177
	v_fmac_f32_e32 v61, v176, v176
	v_mul_f32_e32 v62, v179, v179
	v_fmac_f32_e32 v62, v178, v178
	v_mul_f32_e32 v63, v181, v181
	v_fmac_f32_e32 v63, v180, v180
	v_add_f32_e32 v60, v60, v61
	v_add_f32_e32 v60, v62, v60
	v_add_f32_e32 v60, v63, v60
	v_mov_b32_e32 v192, v60
	s_waitcnt vmcnt(9)
	v_lshlrev_b32_e32 v174, 16, v162
	v_and_b32_e32 v175, 0xffff0000, v162
	v_lshlrev_b32_e32 v176, 16, v163
	v_and_b32_e32 v177, 0xffff0000, v163
	v_lshlrev_b32_e32 v178, 16, v164
	v_and_b32_e32 v179, 0xffff0000, v164
	v_lshlrev_b32_e32 v180, 16, v165
	v_and_b32_e32 v181, 0xffff0000, v165
	global_load_dwordx4 v[162:165], v[182:183], off offset:256
	v_pk_fma_f32 v[174:175], v[52:53], v[210:211], v[174:175]
	v_pk_fma_f32 v[176:177], v[54:55], v[212:213], v[176:177]
	v_pk_fma_f32 v[178:179], v[48:49], v[214:215], v[178:179]
	v_pk_fma_f32 v[180:181], v[50:51], v[216:217], v[180:181]
	v_cvt_pk_bf16_f32 v48, v174, v175
	v_cvt_pk_bf16_f32 v49, v176, v177
	v_cvt_pk_bf16_f32 v50, v178, v179
	v_cvt_pk_bf16_f32 v51, v180, v181
	global_store_dwordx4 v[184:185], v[48:51], off offset:256
	v_mul_f32_e32 v52, v175, v175
	v_fmac_f32_e32 v52, v174, v174
	v_mul_f32_e32 v53, v177, v177
	v_fmac_f32_e32 v53, v176, v176
	v_mul_f32_e32 v54, v179, v179
	v_fmac_f32_e32 v54, v178, v178
	v_mul_f32_e32 v55, v181, v181
	v_fmac_f32_e32 v55, v180, v180
	v_add_f32_e32 v52, v52, v53
	v_add_f32_e32 v52, v54, v52
	v_add_f32_e32 v52, v55, v52
	v_add_f32_e32 v192, v192, v52
	ds_bpermute_b32 v193, v190, v192
	s_waitcnt lgkmcnt(0)
	v_add_f32_e32 v192, v192, v193
	ds_bpermute_b32 v193, v191, v192
	s_waitcnt lgkmcnt(0)
	v_add_f32_e32 v192, v192, v193
	s_and_saveexec_b64 s[26:27], s[4:5]
	global_store_dword v[188:189], v192, off
	s_or_b64 exec, exec, s[26:27]
	v_add_co_u32_e32 v184, vcc, 0x8000, v184
	s_nop 1
	v_addc_co_u32_e32 v185, vcc, 0, v185, vcc
	s_waitcnt vmcnt(9)
	v_lshlrev_b32_e32 v174, 16, v166
	v_and_b32_e32 v175, 0xffff0000, v166
	v_lshlrev_b32_e32 v176, 16, v167
	v_and_b32_e32 v177, 0xffff0000, v167
	v_lshlrev_b32_e32 v178, 16, v168
	v_and_b32_e32 v179, 0xffff0000, v168
	v_lshlrev_b32_e32 v180, 16, v169
	v_and_b32_e32 v181, 0xffff0000, v169
	v_add_co_u32_e32 v182, vcc, 0x8000, v182
	s_nop 1
	v_addc_co_u32_e32 v183, vcc, 0, v183, vcc
	global_load_dwordx4 v[166:169], v[182:183], off
	v_pk_fma_f32 v[174:175], v[44:45], v[202:203], v[174:175]
	v_pk_fma_f32 v[176:177], v[46:47], v[204:205], v[176:177]
	v_pk_fma_f32 v[178:179], v[40:41], v[206:207], v[178:179]
	v_pk_fma_f32 v[180:181], v[42:43], v[208:209], v[180:181]
	v_cvt_pk_bf16_f32 v40, v174, v175
	v_cvt_pk_bf16_f32 v41, v176, v177
	v_cvt_pk_bf16_f32 v42, v178, v179
	v_cvt_pk_bf16_f32 v43, v180, v181
	global_store_dwordx4 v[184:185], v[40:43], off
	v_mul_f32_e32 v44, v175, v175
	v_fmac_f32_e32 v44, v174, v174
	v_mul_f32_e32 v45, v177, v177
	v_fmac_f32_e32 v45, v176, v176
	v_mul_f32_e32 v46, v179, v179
	v_fmac_f32_e32 v46, v178, v178
	v_mul_f32_e32 v47, v181, v181
	v_fmac_f32_e32 v47, v180, v180
	v_add_f32_e32 v44, v44, v45
	v_add_f32_e32 v44, v46, v44
	v_add_f32_e32 v44, v47, v44
	v_mov_b32_e32 v192, v44
	s_waitcnt vmcnt(9)
	v_lshlrev_b32_e32 v174, 16, v170
	v_and_b32_e32 v175, 0xffff0000, v170
	v_lshlrev_b32_e32 v176, 16, v171
	v_and_b32_e32 v177, 0xffff0000, v171
	v_lshlrev_b32_e32 v178, 16, v172
	v_and_b32_e32 v179, 0xffff0000, v172
	v_lshlrev_b32_e32 v180, 16, v173
	v_and_b32_e32 v181, 0xffff0000, v173
	global_load_dwordx4 v[170:173], v[182:183], off offset:256
	v_pk_fma_f32 v[174:175], v[36:37], v[210:211], v[174:175]
	v_pk_fma_f32 v[176:177], v[38:39], v[212:213], v[176:177]
	v_pk_fma_f32 v[178:179], v[32:33], v[214:215], v[178:179]
	v_pk_fma_f32 v[180:181], v[34:35], v[216:217], v[180:181]
	v_cvt_pk_bf16_f32 v32, v174, v175
	v_cvt_pk_bf16_f32 v33, v176, v177
	v_cvt_pk_bf16_f32 v34, v178, v179
	v_cvt_pk_bf16_f32 v35, v180, v181
	global_store_dwordx4 v[184:185], v[32:35], off offset:256
	v_mul_f32_e32 v36, v175, v175
	v_fmac_f32_e32 v36, v174, v174
	v_mul_f32_e32 v37, v177, v177
	v_fmac_f32_e32 v37, v176, v176
	v_mul_f32_e32 v38, v179, v179
	v_fmac_f32_e32 v38, v178, v178
	v_mul_f32_e32 v39, v181, v181
	v_fmac_f32_e32 v39, v180, v180
	v_add_f32_e32 v36, v36, v37
	v_add_f32_e32 v36, v38, v36
	v_add_f32_e32 v36, v39, v36
	v_add_f32_e32 v192, v192, v36
	ds_bpermute_b32 v193, v190, v192
	s_waitcnt lgkmcnt(0)
	v_add_f32_e32 v192, v192, v193
	ds_bpermute_b32 v193, v191, v192
	s_waitcnt lgkmcnt(0)
	v_add_f32_e32 v192, v192, v193
	s_and_saveexec_b64 s[26:27], s[4:5]
	global_store_dword v[188:189], v192, off offset:1024
	s_or_b64 exec, exec, s[26:27]
	v_add_co_u32_e32 v184, vcc, 0x8000, v184
	s_nop 1
	v_addc_co_u32_e32 v185, vcc, 0, v185, vcc
	s_waitcnt vmcnt(9)
	v_lshlrev_b32_e32 v174, 16, v158
	v_and_b32_e32 v175, 0xffff0000, v158
	v_lshlrev_b32_e32 v176, 16, v159
	v_and_b32_e32 v177, 0xffff0000, v159
	v_lshlrev_b32_e32 v178, 16, v160
	v_and_b32_e32 v179, 0xffff0000, v160
	v_lshlrev_b32_e32 v180, 16, v161
	v_and_b32_e32 v181, 0xffff0000, v161
	v_pk_fma_f32 v[174:175], v[28:29], v[202:203], v[174:175]
	v_pk_fma_f32 v[176:177], v[30:31], v[204:205], v[176:177]
	v_pk_fma_f32 v[178:179], v[24:25], v[206:207], v[178:179]
	v_pk_fma_f32 v[180:181], v[26:27], v[208:209], v[180:181]
	v_cvt_pk_bf16_f32 v24, v174, v175
	v_cvt_pk_bf16_f32 v25, v176, v177
	v_cvt_pk_bf16_f32 v26, v178, v179
	v_cvt_pk_bf16_f32 v27, v180, v181
	global_store_dwordx4 v[184:185], v[24:27], off
	v_mul_f32_e32 v28, v175, v175
	v_fmac_f32_e32 v28, v174, v174
	v_mul_f32_e32 v29, v177, v177
	v_fmac_f32_e32 v29, v176, v176
	v_mul_f32_e32 v30, v179, v179
	v_fmac_f32_e32 v30, v178, v178
	v_mul_f32_e32 v31, v181, v181
	v_fmac_f32_e32 v31, v180, v180
	v_add_f32_e32 v28, v28, v29
	v_add_f32_e32 v28, v30, v28
	v_add_f32_e32 v28, v31, v28
	v_mov_b32_e32 v192, v28
	s_waitcnt vmcnt(8)
	v_lshlrev_b32_e32 v174, 16, v162
	v_and_b32_e32 v175, 0xffff0000, v162
	v_lshlrev_b32_e32 v176, 16, v163
	v_and_b32_e32 v177, 0xffff0000, v163
	v_lshlrev_b32_e32 v178, 16, v164
	v_and_b32_e32 v179, 0xffff0000, v164
	v_lshlrev_b32_e32 v180, 16, v165
	v_and_b32_e32 v181, 0xffff0000, v165
	v_pk_fma_f32 v[174:175], v[20:21], v[210:211], v[174:175]
	v_pk_fma_f32 v[176:177], v[22:23], v[212:213], v[176:177]
	v_pk_fma_f32 v[178:179], v[16:17], v[214:215], v[178:179]
	v_pk_fma_f32 v[180:181], v[18:19], v[216:217], v[180:181]
	v_cvt_pk_bf16_f32 v16, v174, v175
	v_cvt_pk_bf16_f32 v17, v176, v177
	v_cvt_pk_bf16_f32 v18, v178, v179
	v_cvt_pk_bf16_f32 v19, v180, v181
	global_store_dwordx4 v[184:185], v[16:19], off offset:256
	v_mul_f32_e32 v20, v175, v175
	v_fmac_f32_e32 v20, v174, v174
	v_mul_f32_e32 v21, v177, v177
	v_fmac_f32_e32 v21, v176, v176
	v_mul_f32_e32 v22, v179, v179
	v_fmac_f32_e32 v22, v178, v178
	v_mul_f32_e32 v23, v181, v181
	v_fmac_f32_e32 v23, v180, v180
	v_add_f32_e32 v20, v20, v21
	v_add_f32_e32 v20, v22, v20
	v_add_f32_e32 v20, v23, v20
	v_add_f32_e32 v192, v192, v20
	ds_bpermute_b32 v193, v190, v192
	s_waitcnt lgkmcnt(0)
	v_add_f32_e32 v192, v192, v193
	ds_bpermute_b32 v193, v191, v192
	s_waitcnt lgkmcnt(0)
	v_add_f32_e32 v192, v192, v193
	s_and_saveexec_b64 s[26:27], s[4:5]
	global_store_dword v[188:189], v192, off offset:2048
	s_or_b64 exec, exec, s[26:27]
	v_add_co_u32_e32 v184, vcc, 0x8000, v184
	s_nop 1
	v_addc_co_u32_e32 v185, vcc, 0, v185, vcc
	s_waitcnt vmcnt(7)
	v_lshlrev_b32_e32 v174, 16, v166
	v_and_b32_e32 v175, 0xffff0000, v166
	v_lshlrev_b32_e32 v176, 16, v167
	v_and_b32_e32 v177, 0xffff0000, v167
	v_lshlrev_b32_e32 v178, 16, v168
	v_and_b32_e32 v179, 0xffff0000, v168
	v_lshlrev_b32_e32 v180, 16, v169
	v_and_b32_e32 v181, 0xffff0000, v169
	v_pk_fma_f32 v[174:175], v[12:13], v[202:203], v[174:175]
	v_pk_fma_f32 v[176:177], v[14:15], v[204:205], v[176:177]
	v_pk_fma_f32 v[178:179], v[8:9], v[206:207], v[178:179]
	v_pk_fma_f32 v[180:181], v[10:11], v[208:209], v[180:181]
	v_cvt_pk_bf16_f32 v8, v174, v175
	v_cvt_pk_bf16_f32 v9, v176, v177
	v_cvt_pk_bf16_f32 v10, v178, v179
	v_cvt_pk_bf16_f32 v11, v180, v181
	global_store_dwordx4 v[184:185], v[8:11], off
	v_mul_f32_e32 v12, v175, v175
	v_fmac_f32_e32 v12, v174, v174
	v_mul_f32_e32 v13, v177, v177
	v_fmac_f32_e32 v13, v176, v176
	v_mul_f32_e32 v14, v179, v179
	v_fmac_f32_e32 v14, v178, v178
	v_mul_f32_e32 v15, v181, v181
	v_fmac_f32_e32 v15, v180, v180
	v_add_f32_e32 v12, v12, v13
	v_add_f32_e32 v12, v14, v12
	v_add_f32_e32 v12, v15, v12
	v_mov_b32_e32 v192, v12
	s_waitcnt vmcnt(6)
	v_lshlrev_b32_e32 v174, 16, v170
	v_and_b32_e32 v175, 0xffff0000, v170
	v_lshlrev_b32_e32 v176, 16, v171
	v_and_b32_e32 v177, 0xffff0000, v171
	v_lshlrev_b32_e32 v178, 16, v172
	v_and_b32_e32 v179, 0xffff0000, v172
	v_lshlrev_b32_e32 v180, 16, v173
	v_and_b32_e32 v181, 0xffff0000, v173
	v_pk_fma_f32 v[174:175], v[4:5], v[210:211], v[174:175]
	v_pk_fma_f32 v[176:177], v[6:7], v[212:213], v[176:177]
	v_pk_fma_f32 v[178:179], v[0:1], v[214:215], v[178:179]
	v_pk_fma_f32 v[180:181], v[2:3], v[216:217], v[180:181]
	v_cvt_pk_bf16_f32 v0, v174, v175
	v_cvt_pk_bf16_f32 v1, v176, v177
	v_cvt_pk_bf16_f32 v2, v178, v179
	v_cvt_pk_bf16_f32 v3, v180, v181
	global_store_dwordx4 v[184:185], v[0:3], off offset:256
	v_mul_f32_e32 v4, v175, v175
	v_fmac_f32_e32 v4, v174, v174
	v_mul_f32_e32 v5, v177, v177
	v_fmac_f32_e32 v5, v176, v176
	v_mul_f32_e32 v6, v179, v179
	v_fmac_f32_e32 v6, v178, v178
	v_mul_f32_e32 v7, v181, v181
	v_fmac_f32_e32 v7, v180, v180
	v_add_f32_e32 v4, v4, v5
	v_add_f32_e32 v4, v6, v4
	v_add_f32_e32 v4, v7, v4
	v_add_f32_e32 v192, v192, v4
	ds_bpermute_b32 v193, v190, v192
	s_waitcnt lgkmcnt(0)
	v_add_f32_e32 v192, v192, v193
	ds_bpermute_b32 v193, v191, v192
	s_waitcnt lgkmcnt(0)
	v_add_f32_e32 v192, v192, v193
	s_and_saveexec_b64 s[26:27], s[4:5]
	global_store_dword v[188:189], v192, off offset:3072
	s_or_b64 exec, exec, s[26:27]
	s_and_b64 vcc, exec, s[6:7]
	s_mov_b64 s[6:7], -1
	s_cbranch_vccnz .LBB0_1846
	s_andn2_b64 vcc, exec, s[10:11]
	s_cbranch_vccnz .LBB0_1845
	s_barrier
	s_branch .LBB0_1845
